# P2 split back to 160 GEMM workgroups / 96 quantizer workgroups (tile phase of P8 is now short, so more weight quantization inside P2 pays); otherwise v81
# speedup vs baseline: 1.0270x; 1.0049x over previous
; #define LAS __attribute__((address_space(3)))
; #define Q_GRAB() (((stop != nullptr && xb_ld(stop) >= thr) || (quota > 0 && qleft-- <= 0)) ? (unsigned)hi : (unsigned)lo + atomicAdd(cnt, 1u))
;     ...
;         unsigned nxt = 0u; if (tid == 0) nxt = Q_GRAB();
;         signed char* Qc = Qp; float* csc = csp; const bool f8c = f8; const float qmax = f8c ? 448.0f : 127.0f, qinv = f8c ? (1.0f / 448.0f) : (1.0f / 127.0f);
;         f32x4 mx = {0.f, 0.f, 0.f, 0.f};
; #pragma unroll
;         for (int g = 0; g < 8; ++g)
; #pragma unroll
;             for (int r = 0; r < 4; ++r) { mx[0] = fmaxf(mx[0], fabsf(v[g][r][0])); mx[1] = fmaxf(mx[1], fabsf(v[g][r][1])); mx[2] = fmaxf(mx[2], fabsf(v[g][r][2])); mx[3] = fmaxf(mx[3], fabsf(v[g][r][3])); }
; #pragma unroll
;         for (int c = 0; c < 4; ++c) { float m = mx[c]; m = fmaxf(m, __shfl_xor(m, 8)); m = fmaxf(m, __shfl_xor(m, 16)); m = fmaxf(m, __shfl_xor(m, 32)); mx[c] = m; }
;         if (tid == 0) MISC[2] = nxt;
;         if (kr == 0) *(LAS f32x4*)(smax + wave * 32 + 4 * n4) = mx;
.LBB0_334:
	s_waitcnt vmcnt(10)
	v_max3_f32 v130, |v2|, 0, |v6|
	s_waitcnt vmcnt(8)
	v_max3_f32 v130, v130, |v10|, |v14|
	v_max3_f32 v130, v130, |v18|, |v22|
	v_max3_f32 v130, v130, |v26|, |v30|
	v_max3_f32 v130, v130, |v34|, |v38|
	v_max3_f32 v130, v130, |v42|, |v46|
	v_max3_f32 v131, |v3|, 0, |v7|
	v_max3_f32 v130, v130, |v50|, |v54|
	v_max3_f32 v132, |v4|, 0, |v8|
	v_max3_f32 v131, v131, |v11|, |v15|
	v_max3_f32 v130, v130, |v58|, |v62|
	v_max3_f32 v132, v132, |v12|, |v16|
	v_max3_f32 v131, v131, |v19|, |v23|
	v_max3_f32 v130, v130, |v66|, |v70|
	v_max3_f32 v132, v132, |v20|, |v24|
	v_max3_f32 v131, v131, |v27|, |v31|
	v_max3_f32 v130, v130, |v74|, |v78|
	v_max3_f32 v132, v132, |v28|, |v32|
	v_max3_f32 v131, v131, |v35|, |v39|
	v_max3_f32 v130, v130, |v82|, |v86|
	v_max3_f32 v132, v132, |v36|, |v40|
	v_max3_f32 v131, v131, |v43|, |v47|
	v_max3_f32 v130, v130, |v90|, |v94|
	v_max3_f32 v132, v132, |v44|, |v48|
	v_max3_f32 v131, v131, |v51|, |v55|
	s_waitcnt vmcnt(6)
	v_max3_f32 v130, v130, |v98|, |v102|
	v_max3_f32 v133, |v5|, 0, |v9|
	v_max3_f32 v132, v132, |v52|, |v56|
	v_max3_f32 v131, v131, |v59|, |v63|
	s_waitcnt vmcnt(4)
	v_max3_f32 v130, v130, |v106|, |v110|
	v_max3_f32 v133, v133, |v13|, |v17|
	v_max3_f32 v132, v132, |v60|, |v64|
	v_max3_f32 v131, v131, |v67|, |v71|
	s_waitcnt vmcnt(2)
	v_max3_f32 v130, v130, |v114|, |v118|
	v_max3_f32 v133, v133, |v21|, |v25|
	v_max3_f32 v132, v132, |v68|, |v72|
	v_max3_f32 v131, v131, |v75|, |v79|
	s_waitcnt vmcnt(0)
	v_max3_f32 v130, v130, |v122|, |v126|
	v_max3_f32 v133, v133, |v29|, |v33|
	v_max3_f32 v132, v132, |v76|, |v80|
	v_max3_f32 v131, v131, |v83|, |v87|
	v_max3_f32 v133, v133, |v37|, |v41|
	v_max3_f32 v132, v132, |v84|, |v88|
	v_max3_f32 v131, v131, |v91|, |v95|
	v_max3_f32 v133, v133, |v45|, |v49|
	v_max3_f32 v132, v132, |v92|, |v96|
	v_max3_f32 v131, v131, |v99|, |v103|
	v_max3_f32 v133, v133, |v53|, |v57|
	v_max3_f32 v132, v132, |v100|, |v104|
	v_max3_f32 v131, v131, |v107|, |v111|
	v_max3_f32 v133, v133, |v61|, |v65|
	v_max3_f32 v132, v132, |v108|, |v112|
	v_max3_f32 v131, v131, |v115|, |v119|
	v_max3_f32 v133, v133, |v69|, |v73|
	v_max3_f32 v132, v132, |v116|, |v120|
	v_max3_f32 v131, v131, |v123|, |v127|
	v_max3_f32 v133, v133, |v77|, |v81|
	v_max3_f32 v135, v132, |v124|, |v128|
	v_max3_f32 v133, v133, |v85|, |v89|
	v_max3_f32 v133, v133, |v93|, |v97|
	v_max3_f32 v133, v133, |v101|, |v105|
	v_max3_f32 v133, v133, |v109|, |v113|
	v_max3_f32 v133, v133, |v117|, |v121|
	v_max3_f32 v133, v133, |v125|, |v129|
	v_mov_b32_e32 v132, v135
	s_nop 1
	v_max_f32_dpp v130, v130, v130 row_ror:8 row_mask:0xf bank_mask:0xf
	v_max_f32_dpp v131, v131, v131 row_ror:8 row_mask:0xf bank_mask:0xf
	v_max_f32_dpp v132, v132, v132 row_ror:8 row_mask:0xf bank_mask:0xf
	v_max_f32_dpp v133, v133, v133 row_ror:8 row_mask:0xf bank_mask:0xf
	v_mov_b32_e32 v134, v130
	v_mov_b32_e32 v136, v131
	v_mov_b32_e32 v137, v132
	v_mov_b32_e32 v138, v133
	s_nop 1
	v_permlane16_swap_b32 v130, v134
	v_permlane16_swap_b32 v131, v136
	v_permlane16_swap_b32 v132, v137
	v_permlane16_swap_b32 v133, v138
	v_max_f32_e32 v130, v130, v134
	v_max_f32_e32 v131, v131, v136
	v_max_f32_e32 v132, v132, v137
	v_max_f32_e32 v133, v133, v138
	v_mov_b32_e32 v134, v130
	v_mov_b32_e32 v136, v131
	v_mov_b32_e32 v137, v132
	v_mov_b32_e32 v138, v133
	s_nop 1
	v_permlane32_swap_b32 v130, v134
	v_permlane32_swap_b32 v131, v136
	v_permlane32_swap_b32 v132, v137
	v_permlane32_swap_b32 v133, v138
	v_max_f32_e32 v130, v130, v134
	v_max_f32_e32 v131, v131, v136
	v_max_f32_e32 v132, v132, v137
	v_max_f32_e32 v133, v133, v138
	s_and_saveexec_b64 s[6:7], s[40:41]
	v_add_u32_e32 v1, 0x1c8, v199
	v_cmp_lt_u32_e32 vcc, 55, v201
	s_mov_b64 s[12:13], vcc
	v_cmp_le_u32_e32 vcc, 0x19c8, v1
	s_or_b64 s[12:13], s[12:13], vcc
	v_mov_b32_e32 v199, 0x1800
	s_andn2_b64 exec, exec, s[12:13]
	v_mov_b32_e32 v203, 1
	global_atomic_add v199, v171, v203, s[20:21] sc0
	s_and_b64 exec, s[6:7], s[40:41]
	global_load_dword v201, v171, s[22:23] sc1
	v_mov_b32_e32 v138, s75
	ds_write_b32 v138, v1
	s_or_b64 exec, exec, s[6:7]
	s_and_saveexec_b64 s[6:7], s[4:5]
	s_cbranch_execz .LBB0_343
	v_add_u32_e32 v1, s44, v169
	ds_write_b128 v1, v[130:133]
